# baseline (speedup 1.0000x reference)
_Z7k_gatesPKfPKtS0_PhPf:
	s_load_dwordx8 s[4:11], s[0:1], 0x0
	v_and_b32_e32 v1, 15, v0
	s_lshl_b32 s2, s2, 4
	v_or_b32_e32 v68, s2, v1
	v_ashrrev_i32_e32 v69, 31, v68
	v_lshrrev_b32_e32 v74, 6, v0
	v_lshlrev_b64 v[2:3], 12, v[68:69]
	s_waitcnt lgkmcnt(0)
	v_lshl_add_u64 v[2:3], s[4:5], 0, v[2:3]
	v_lshlrev_b32_e32 v66, 10, v74
	v_mov_b32_e32 v67, 0
	v_and_b32_e32 v75, 48, v0
	v_lshl_add_u64 v[2:3], v[2:3], 0, v[66:67]
	v_lshlrev_b32_e32 v4, 2, v75
	v_mov_b32_e32 v5, v67
	v_lshl_add_u64 v[14:15], v[2:3], 0, v[4:5]
	v_lshlrev_b32_e32 v70, 4, v0
	v_cmp_gt_u32_e32 vcc, 16, v0
	s_add_u32 s14, s6, 0x8000
	s_addc_u32 s15, s7, 0
	s_and_saveexec_b64 s[12:13], vcc
	s_cbranch_execz .Lg_skip9a
	global_load_dwordx4 v[116:119], v70, s[14:15]
.Lg_skip9a:
	s_mov_b64 exec, s[12:13]
	global_load_dwordx4 v[84:87], v70, s[6:7]
	s_add_u32 s6, s6, 0x1000
	s_addc_u32 s7, s7, 0
	global_load_dwordx4 v[88:91], v70, s[6:7]
	s_add_u32 s6, s6, 0x1000
	s_addc_u32 s7, s7, 0
	global_load_dwordx4 v[92:95], v70, s[6:7]
	s_add_u32 s6, s6, 0x1000
	s_addc_u32 s7, s7, 0
	global_load_dwordx4 v[96:99], v70, s[6:7]
	s_add_u32 s6, s6, 0x1000
	s_addc_u32 s7, s7, 0
	global_load_dwordx4 v[100:103], v70, s[6:7]
	s_add_u32 s6, s6, 0x1000
	s_addc_u32 s7, s7, 0
	global_load_dwordx4 v[104:107], v70, s[6:7]
	s_add_u32 s6, s6, 0x1000
	s_addc_u32 s7, s7, 0
	global_load_dwordx4 v[108:111], v70, s[6:7]
	s_add_u32 s6, s6, 0x1000
	s_addc_u32 s7, s7, 0
	global_load_dwordx4 v[112:115], v70, s[6:7]
	global_load_dwordx4 v[50:53], v[14:15], off offset:48 nt
	global_load_dwordx4 v[54:57], v[14:15], off offset:32 nt
	global_load_dwordx4 v[58:61], v[14:15], off offset:16 nt
	global_load_dwordx4 v[62:65], v[14:15], off nt
	global_load_dwordx4 v[34:37], v[14:15], off offset:304 nt
	global_load_dwordx4 v[38:41], v[14:15], off offset:288 nt
	global_load_dwordx4 v[42:45], v[14:15], off offset:272 nt
	global_load_dwordx4 v[46:49], v[14:15], off offset:256 nt
	global_load_dwordx4 v[18:21], v[14:15], off offset:560 nt
	global_load_dwordx4 v[22:25], v[14:15], off offset:544 nt
	global_load_dwordx4 v[26:29], v[14:15], off offset:528 nt
	global_load_dwordx4 v[30:33], v[14:15], off offset:512 nt
	global_load_dwordx4 v[2:5], v[14:15], off offset:816 nt
	global_load_dwordx4 v[6:9], v[14:15], off offset:800 nt
	global_load_dwordx4 v[10:13], v[14:15], off offset:784 nt
	s_nop 0
	global_load_dwordx4 v[14:17], v[14:15], off offset:768 nt
	s_load_dwordx2 s[4:5], s[0:1], 0x20
	v_lshlrev_b32_e32 v76, 8, v74
	s_waitcnt vmcnt(16)
	ds_write_b128 v70, v[84:87]
	ds_write_b128 v70, v[88:91] offset:4096
	ds_write_b128 v70, v[92:95] offset:8192
	ds_write_b128 v70, v[96:99] offset:12288
	ds_write_b128 v70, v[100:103] offset:16384
	ds_write_b128 v70, v[104:107] offset:20480
	ds_write_b128 v70, v[108:111] offset:24576
	ds_write_b128 v70, v[112:115] offset:28672
	v_cmp_gt_u32_e32 vcc, 16, v0
	s_and_saveexec_b64 s[12:13], vcc
	s_cbranch_execz .Lg_skip9b
	ds_write_b128 v70, v[116:119] offset:32768
.Lg_skip9b:
	s_mov_b64 exec, s[12:13]
	s_waitcnt vmcnt(0)
	v_mov_b32_e32 v79, 0
	v_lshlrev_b32_e32 v72, 1, v76
	v_mov_b32_e32 v76, v79
	v_cvt_scalef32_pk_fp4_f32 v76, v62, v63, 0.5
	v_mul_u32_u24_e32 v71, 0x810, v1
	v_lshlrev_b32_e32 v73, 1, v75
	v_cvt_scalef32_pk_fp4_f32 v76, v64, v65, 0.5 op_sel:[0,0,1,0]
	v_add3_u32 v71, v71, v72, v73
	v_cvt_scalef32_pk_fp4_f32 v76, v58, v59, 0.5 op_sel:[0,0,0,1]
	s_waitcnt lgkmcnt(0)
	s_barrier
	v_cvt_scalef32_pk_fp4_f32 v76, v60, v61, 0.5 op_sel:[0,0,1,1]
	v_cvt_pk_f16_f32 v62, v62, v63
	v_cvt_pk_f16_f32 v63, v64, v65
	v_cvt_pk_f16_f32 v64, v58, v59
	v_cvt_pk_f16_f32 v65, v60, v61
	ds_read_b128 v[58:61], v71
	v_mov_b32_e32 v77, v79
	v_cvt_scalef32_pk_fp4_f32 v77, v54, v55, 0.5
	v_lshlrev_b32_e32 v78, 7, v74
	v_cvt_scalef32_pk_fp4_f32 v77, v56, v57, 0.5 op_sel:[0,0,1,0]
	v_cvt_pk_f16_f32 v54, v54, v55
	v_cvt_pk_f16_f32 v55, v56, v57
	v_cvt_pk_f16_f32 v56, v50, v51
	v_cvt_pk_f16_f32 v57, v52, v53
	ds_read_b128 v[72:75], v71 offset:16
	s_waitcnt lgkmcnt(1)
	v_mfma_f32_16x16x32_f16 a[0:3], v[62:65], v[58:61], 0
	v_cvt_scalef32_pk_fp4_f32 v77, v50, v51, 0.5 op_sel:[0,0,0,1]
	v_lshlrev_b64 v[68:69], 9, v[68:69]
	v_cvt_scalef32_pk_fp4_f32 v77, v52, v53, 0.5 op_sel:[0,0,1,1]
	s_waitcnt lgkmcnt(0)
	v_mfma_f32_16x16x32_f16 a[0:3], v[54:57], v[72:75], a[0:3]
	v_mov_b32_e32 v54, v79
	v_cvt_scalef32_pk_fp4_f32 v54, v46, v47, 0.5
	v_cvt_scalef32_pk_fp4_f32 v54, v48, v49, 0.5 op_sel:[0,0,1,0]
	v_cvt_pk_f16_f32 v46, v46, v47
	v_cvt_scalef32_pk_fp4_f32 v54, v42, v43, 0.5 op_sel:[0,0,0,1]
	v_cvt_pk_f16_f32 v47, v48, v49
	v_cvt_scalef32_pk_fp4_f32 v54, v44, v45, 0.5 op_sel:[0,0,1,1]
	v_cvt_pk_f16_f32 v48, v42, v43
	v_cvt_pk_f16_f32 v49, v44, v45
	ds_read_b128 v[42:45], v71 offset:128
	ds_read_b128 v[50:53], v71 offset:144
	v_mov_b32_e32 v55, v79
	v_cvt_scalef32_pk_fp4_f32 v55, v38, v39, 0.5
	v_cvt_scalef32_pk_fp4_f32 v55, v40, v41, 0.5 op_sel:[0,0,1,0]
	v_cvt_pk_f16_f32 v38, v38, v39
	v_cvt_pk_f16_f32 v39, v40, v41
	v_cvt_pk_f16_f32 v40, v34, v35
	v_cvt_pk_f16_f32 v41, v36, v37
	s_waitcnt lgkmcnt(1)
	v_mfma_f32_16x16x32_f16 a[0:3], v[46:49], v[42:45], a[0:3]
	v_bfe_u32 v67, v0, 4, 2
	v_lshl_add_u64 v[68:69], s[10:11], 0, v[68:69]
	v_lshl_add_u64 v[68:69], v[68:69], 0, v[78:79]
	s_waitcnt lgkmcnt(0)
	v_mfma_f32_16x16x32_f16 a[0:3], v[38:41], v[50:53], a[0:3]
	v_mov_b32_e32 v38, v79
	v_cvt_scalef32_pk_fp4_f32 v38, v30, v31, 0.5
	v_cvt_scalef32_pk_fp4_f32 v38, v32, v33, 0.5 op_sel:[0,0,1,0]
	v_cvt_pk_f16_f32 v30, v30, v31
	v_cvt_scalef32_pk_fp4_f32 v38, v26, v27, 0.5 op_sel:[0,0,0,1]
	v_cvt_pk_f16_f32 v31, v32, v33
	v_cvt_scalef32_pk_fp4_f32 v38, v28, v29, 0.5 op_sel:[0,0,1,1]
	v_cvt_pk_f16_f32 v32, v26, v27
	v_cvt_pk_f16_f32 v33, v28, v29
	ds_read_b128 v[26:29], v71 offset:256
	v_mov_b32_e32 v39, v79
	v_lshlrev_b32_e32 v78, 3, v67
	v_cvt_scalef32_pk_fp4_f32 v55, v34, v35, 0.5 op_sel:[0,0,0,1]
	v_cvt_scalef32_pk_fp4_f32 v39, v22, v23, 0.5
	v_lshl_add_u64 v[68:69], v[68:69], 0, v[78:79]
	v_cvt_scalef32_pk_fp4_f32 v55, v36, v37, 0.5 op_sel:[0,0,1,1]
	v_cvt_scalef32_pk_fp4_f32 v39, v24, v25, 0.5 op_sel:[0,0,1,0]
	v_cvt_pk_f16_f32 v22, v22, v23
	v_cvt_pk_f16_f32 v23, v24, v25
	v_cvt_pk_f16_f32 v24, v18, v19
	v_cvt_pk_f16_f32 v25, v20, v21
	ds_read_b128 v[34:37], v71 offset:272
	v_mov_b32_e32 v78, v79
	s_waitcnt lgkmcnt(1)
	v_mfma_f32_16x16x32_f16 a[0:3], v[30:33], v[26:29], a[0:3]
	v_cvt_scalef32_pk_fp4_f32 v78, v14, v15, 0.5
	v_cvt_scalef32_pk_fp4_f32 v78, v16, v17, 0.5 op_sel:[0,0,1,0]
	v_cvt_pk_f16_f32 v14, v14, v15
	v_cvt_scalef32_pk_fp4_f32 v78, v10, v11, 0.5 op_sel:[0,0,0,1]
	v_cvt_pk_f16_f32 v15, v16, v17
	v_cvt_scalef32_pk_fp4_f32 v78, v12, v13, 0.5 op_sel:[0,0,1,1]
	v_cvt_pk_f16_f32 v16, v10, v11
	v_cvt_pk_f16_f32 v17, v12, v13
	ds_read_b128 v[10:13], v71 offset:384
	s_waitcnt lgkmcnt(1)
	v_mfma_f32_16x16x32_f16 a[0:3], v[22:25], v[34:37], a[0:3]
	v_cvt_scalef32_pk_fp4_f32 v39, v18, v19, 0.5 op_sel:[0,0,0,1]
	v_cvt_scalef32_pk_fp4_f32 v79, v6, v7, 0.5
	v_cvt_scalef32_pk_fp4_f32 v39, v20, v21, 0.5 op_sel:[0,0,1,1]
	v_cvt_scalef32_pk_fp4_f32 v79, v8, v9, 0.5 op_sel:[0,0,1,0]
	v_cvt_pk_f16_f32 v6, v6, v7
	v_cvt_pk_f16_f32 v7, v8, v9
	v_cvt_pk_f16_f32 v8, v2, v3
	v_cvt_pk_f16_f32 v9, v4, v5
	ds_read_b128 v[18:21], v71 offset:400
	s_waitcnt lgkmcnt(1)
	v_mfma_f32_16x16x32_f16 a[0:3], v[14:17], v[10:13], a[0:3]
	v_cvt_scalef32_pk_fp4_f32 v79, v2, v3, 0.5 op_sel:[0,0,0,1]
	v_and_b32_e32 v70, 63, v0
	v_cvt_scalef32_pk_fp4_f32 v79, v4, v5, 0.5 op_sel:[0,0,1,1]
	s_waitcnt lgkmcnt(0)
	v_mfma_f32_16x16x32_f16 a[0:3], v[6:9], v[18:21], a[0:3]
	v_cmp_gt_u32_e32 vcc, 64, v0
	v_cmp_lt_u32_e64 s[0:1], 63, v0
	global_store_dwordx2 v[68:69], v[76:77], off
	global_store_dwordx2 v[68:69], v[54:55], off offset:32
	global_store_dwordx2 v[68:69], v[38:39], off offset:64
	global_store_dwordx2 v[68:69], v[78:79], off offset:96
	s_nop 1
	v_accvgpr_read_b32 v5, a3
	v_accvgpr_read_b32 v4, a2
	v_accvgpr_read_b32 v3, a1
	v_accvgpr_read_b32 v2, a0
	s_and_saveexec_b64 s[6:7], s[0:1]
	v_lshl_or_b32 v6, v70, 4, v66
	ds_write_b128 v6, a[0:3] offset:32000
	s_or_b64 exec, exec, s[6:7]
	s_waitcnt lgkmcnt(0)
	s_barrier
	s_and_saveexec_b64 s[0:1], vcc
	s_cbranch_execz .LBB1_6
	v_lshlrev_b32_e32 v1, 2, v1
	global_load_dword v20, v1, s[8:9]
	v_lshlrev_b32_e32 v14, 4, v70
	v_mbcnt_lo_u32_b32 v18, -1, 0
	v_lshlrev_b32_e32 v19, 11, v0
	ds_read_b128 v[6:9], v14 offset:33024
	ds_read_b128 v[10:13], v14 offset:34048
	ds_read_b128 v[14:17], v14 offset:35072
	v_mbcnt_hi_u32_b32 v22, -1, v18
	v_mov_b32_e32 v1, 0
	s_ashr_i32 s3, s2, 31
	v_and_b32_e32 v21, 7, v0
	v_and_b32_e32 v0, 0x4000, v19
	v_and_b32_e32 v24, 64, v22
	v_xor_b32_e32 v23, 1, v22
	v_lshl_add_u64 v[18:19], v[0:1], 0, s[2:3]
	v_lshlrev_b32_e32 v0, 2, v21
	v_add_u32_e32 v21, 64, v24
	v_xor_b32_e32 v25, 2, v22
	v_cmp_lt_i32_e32 vcc, v23, v21
	s_waitcnt lgkmcnt(2)
	v_add_f32_e32 v2, v2, v6
	v_xor_b32_e32 v26, 4, v22
	v_cndmask_b32_e32 v23, v22, v23, vcc
	v_cmp_lt_i32_e32 vcc, v25, v21
	s_waitcnt lgkmcnt(1)
	v_add_f32_e32 v2, v10, v2
	s_waitcnt lgkmcnt(0)
	v_add_f32_e32 v2, v14, v2
	v_cndmask_b32_e32 v24, v22, v25, vcc
	v_cmp_lt_i32_e32 vcc, v26, v21
	v_add_f32_e32 v3, v3, v7
	v_add_f32_e32 v3, v11, v3
	v_cndmask_b32_e32 v21, v22, v26, vcc
	v_lshlrev_b32_e32 v22, 2, v23
	v_add_f32_e32 v3, v15, v3
	v_lshlrev_b32_e32 v10, 2, v24
	v_add_f32_e32 v4, v4, v8
	v_add_f32_e32 v5, v5, v9
	v_add_f32_e32 v4, v12, v4
	v_add_f32_e32 v5, v13, v5
	v_add_f32_e32 v4, v16, v4
	v_add_f32_e32 v5, v17, v5
	v_lshlrev_b32_e32 v15, 2, v21
	v_lshl_or_b32 v18, v67, 2, v18
	v_lshl_add_u64 v[0:1], s[4:5], 0, v[0:1]
	v_lshlrev_b64 v[18:19], 5, v[18:19]
	v_lshl_add_u64 v[0:1], v[0:1], 0, v[18:19]
	s_waitcnt vmcnt(0)
	v_add_f32_e32 v2, v20, v2
	ds_bpermute_b32 v6, v22, v2
	v_add_f32_e32 v3, v20, v3
	ds_bpermute_b32 v7, v22, v3
	v_add_f32_e32 v4, v20, v4
	v_add_f32_e32 v5, v20, v5
	s_waitcnt lgkmcnt(1)
	v_max_f32_e32 v6, v6, v6
	v_max_f32_e32 v6, v2, v6
	ds_bpermute_b32 v11, v10, v6
	s_waitcnt lgkmcnt(1)
	v_max_f32_e32 v7, v7, v7
	v_max_f32_e32 v7, v3, v7
	ds_bpermute_b32 v12, v10, v7
	ds_bpermute_b32 v8, v22, v4
	s_waitcnt lgkmcnt(2)
	v_max_f32_e32 v11, v11, v11
	ds_bpermute_b32 v9, v22, v5
	v_max_f32_e32 v6, v6, v11
	ds_bpermute_b32 v11, v15, v6
	s_waitcnt lgkmcnt(3)
	v_max_f32_e32 v12, v12, v12
	s_waitcnt lgkmcnt(2)
	v_max_f32_e32 v8, v8, v8
	v_max_f32_e32 v7, v7, v12
	s_waitcnt lgkmcnt(1)
	v_max_f32_e32 v9, v9, v9
	v_max_f32_e32 v8, v4, v8
	ds_bpermute_b32 v12, v15, v7
	v_max_f32_e32 v9, v5, v9
	ds_bpermute_b32 v13, v10, v8
	s_waitcnt lgkmcnt(2)
	v_max_f32_e32 v11, v11, v11
	ds_bpermute_b32 v14, v10, v9
	v_max_f32_e32 v6, v6, v11
	v_sub_f32_e32 v2, v2, v6
	v_mul_f32_e32 v2, 0x3fb8aa3b, v2
	s_waitcnt lgkmcnt(2)
	v_max_f32_e32 v12, v12, v12
	v_exp_f32_e32 v2, v2
	s_waitcnt lgkmcnt(1)
	v_max_f32_e32 v13, v13, v13
	v_max_f32_e32 v7, v7, v12
	s_waitcnt lgkmcnt(0)
	v_max_f32_e32 v14, v14, v14
	v_max_f32_e32 v8, v8, v13
	v_sub_f32_e32 v3, v3, v7
	v_max_f32_e32 v9, v9, v14
	ds_bpermute_b32 v13, v15, v8
	v_mul_f32_e32 v3, 0x3fb8aa3b, v3
	ds_bpermute_b32 v14, v15, v9
	v_exp_f32_e32 v3, v3
	ds_bpermute_b32 v6, v22, v2
	s_waitcnt lgkmcnt(2)
	v_max_f32_e32 v13, v13, v13
	v_max_f32_e32 v8, v8, v13
	ds_bpermute_b32 v7, v22, v3
	s_waitcnt lgkmcnt(2)
	v_max_f32_e32 v14, v14, v14
	s_waitcnt lgkmcnt(1)
	v_add_f32_e32 v6, v2, v6
	v_sub_f32_e32 v4, v4, v8
	v_max_f32_e32 v8, v9, v14
	ds_bpermute_b32 v9, v10, v6
	s_waitcnt lgkmcnt(1)
	v_add_f32_e32 v7, v3, v7
	ds_bpermute_b32 v11, v10, v7
	v_mul_f32_e32 v4, 0x3fb8aa3b, v4
	v_exp_f32_e32 v4, v4
	s_waitcnt lgkmcnt(1)
	v_add_f32_e32 v6, v6, v9
	ds_bpermute_b32 v9, v15, v6
	s_waitcnt lgkmcnt(1)
	v_add_f32_e32 v7, v7, v11
	ds_bpermute_b32 v11, v15, v7
	v_sub_f32_e32 v5, v5, v8
	ds_bpermute_b32 v8, v22, v4
	s_waitcnt lgkmcnt(2)
	v_add_f32_e32 v6, v6, v9
	v_div_scale_f32 v9, s[0:1], v6, v6, v2
	v_rcp_f32_e32 v14, v9
	s_waitcnt lgkmcnt(1)
	v_add_f32_e32 v7, v7, v11
	v_div_scale_f32 v13, s[0:1], v7, v7, v3
	v_rcp_f32_e32 v16, v13
	v_fma_f32 v18, -v9, v14, 1.0
	v_div_scale_f32 v11, vcc, v2, v6, v2
	v_fmac_f32_e32 v14, v18, v14
	v_mul_f32_e32 v5, 0x3fb8aa3b, v5
	v_mul_f32_e32 v18, v11, v14
	s_waitcnt lgkmcnt(0)
	v_add_f32_e32 v8, v4, v8
	v_exp_f32_e32 v5, v5
	v_fma_f32 v20, -v9, v18, v11
	ds_bpermute_b32 v12, v10, v8
	v_fma_f32 v19, -v13, v16, 1.0
	v_fmac_f32_e32 v18, v20, v14
	v_div_scale_f32 v17, s[0:1], v3, v7, v3
	v_fmac_f32_e32 v16, v19, v16
	v_fma_f32 v9, -v9, v18, v11
	v_mul_f32_e32 v19, v17, v16
	v_div_fmas_f32 v9, v9, v14, v18
	v_fma_f32 v21, -v13, v19, v17
	v_div_fixup_f32 v2, v9, v6, v2
	ds_bpermute_b32 v6, v22, v5
	v_fmac_f32_e32 v19, v21, v16
	s_waitcnt lgkmcnt(1)
	v_add_f32_e32 v8, v8, v12
	v_fma_f32 v11, -v13, v19, v17
	s_mov_b64 vcc, s[0:1]
	ds_bpermute_b32 v12, v15, v8
	global_store_dword v[0:1], v2, off
	v_div_fmas_f32 v2, v11, v16, v19
	v_div_fixup_f32 v2, v2, v7, v3
	global_store_dword v[0:1], v2, off offset:32
	s_waitcnt lgkmcnt(1)
	v_add_f32_e32 v2, v5, v6
	ds_bpermute_b32 v6, v10, v2
	s_waitcnt lgkmcnt(1)
	v_add_f32_e32 v3, v8, v12
	v_div_scale_f32 v7, s[0:1], v3, v3, v4
	v_rcp_f32_e32 v8, v7
	s_waitcnt lgkmcnt(0)
	v_add_f32_e32 v2, v2, v6
	ds_bpermute_b32 v6, v15, v2
	v_fma_f32 v9, -v7, v8, 1.0
	v_fmac_f32_e32 v8, v9, v8
	v_div_scale_f32 v9, vcc, v4, v3, v4
	v_mul_f32_e32 v10, v9, v8
	v_fma_f32 v11, -v7, v10, v9
	s_waitcnt lgkmcnt(0)
	v_add_f32_e32 v2, v2, v6
	v_fmac_f32_e32 v10, v11, v8
	v_div_scale_f32 v6, s[0:1], v2, v2, v5
	v_fma_f32 v7, -v7, v10, v9
	v_rcp_f32_e32 v9, v6
	v_div_fmas_f32 v7, v7, v8, v10
	v_div_fixup_f32 v3, v7, v3, v4
	global_store_dword v[0:1], v3, off offset:64
	v_fma_f32 v3, -v6, v9, 1.0
	v_fmac_f32_e32 v9, v3, v9
	v_div_scale_f32 v3, vcc, v5, v2, v5
	v_mul_f32_e32 v4, v3, v9
	v_fma_f32 v7, -v6, v4, v3
	v_fmac_f32_e32 v4, v7, v9
	v_fma_f32 v3, -v6, v4, v3
	v_div_fmas_f32 v3, v3, v9, v4
	v_div_fixup_f32 v2, v3, v2, v5
	global_store_dword v[0:1], v2, off offset:96

	.amdhsa_kernel _Z7k_gatesPKfPKtS0_PhPf
		.amdhsa_group_segment_fixed_size 36096
		.amdhsa_private_segment_fixed_size 0
		.amdhsa_kernarg_size 40
		.amdhsa_user_sgpr_count 2
		.amdhsa_user_sgpr_dispatch_ptr 0
		.amdhsa_user_sgpr_queue_ptr 0
		.amdhsa_user_sgpr_kernarg_segment_ptr 1
		.amdhsa_user_sgpr_dispatch_id 0
		.amdhsa_user_sgpr_kernarg_preload_length 0
		.amdhsa_user_sgpr_kernarg_preload_offset 0
		.amdhsa_user_sgpr_private_segment_size 0
		.amdhsa_uses_dynamic_stack 0
		.amdhsa_enable_private_segment 0
		.amdhsa_system_sgpr_workgroup_id_x 1
		.amdhsa_system_sgpr_workgroup_id_y 0
		.amdhsa_system_sgpr_workgroup_id_z 0
		.amdhsa_system_sgpr_workgroup_info 0
		.amdhsa_system_vgpr_workitem_id 0
		.amdhsa_next_free_vgpr 124
		.amdhsa_next_free_sgpr 96
		.amdhsa_accum_offset 120
		.amdhsa_reserve_vcc 1
		.amdhsa_float_round_mode_32 0
		.amdhsa_float_round_mode_16_64 0
		.amdhsa_float_denorm_mode_32 3
		.amdhsa_float_denorm_mode_16_64 3
		.amdhsa_dx10_clamp 1
		.amdhsa_ieee_mode 1
		.amdhsa_fp16_overflow 0
		.amdhsa_tg_split 0
		.amdhsa_exception_fp_ieee_invalid_op 0
		.amdhsa_exception_fp_denorm_src 0
		.amdhsa_exception_fp_ieee_div_zero 0
		.amdhsa_exception_fp_ieee_overflow 0
		.amdhsa_exception_fp_ieee_underflow 0
		.amdhsa_exception_fp_ieee_inexact 0
		.amdhsa_exception_int_div_zero 0
	.end_amdhsa_kernel

.Lfunc_end1:
	.size	_Z7k_gatesPKfPKtS0_PhPf, .Lfunc_end1-_Z7k_gatesPKfPKtS0_PhPf
	.set _Z7k_gatesPKfPKtS0_PhPf.num_vgpr, 120
	.set _Z7k_gatesPKfPKtS0_PhPf.num_agpr, 4
	.set _Z7k_gatesPKfPKtS0_PhPf.numbered_sgpr, 12
	.set _Z7k_gatesPKfPKtS0_PhPf.num_named_barrier, 0
	.set _Z7k_gatesPKfPKtS0_PhPf.private_seg_size, 0
	.set _Z7k_gatesPKfPKtS0_PhPf.uses_vcc, 1
	.set _Z7k_gatesPKfPKtS0_PhPf.uses_flat_scratch, 0
	.set _Z7k_gatesPKfPKtS0_PhPf.has_dyn_sized_stack, 0
	.set _Z7k_gatesPKfPKtS0_PhPf.has_recursion, 0
	.set _Z7k_gatesPKfPKtS0_PhPf.has_indirect_call, 0

_Z6k_gemmI4Epi8ILi0ELb1ELb1EEEv4GemmT_iiii:
	s_load_dwordx4 s[4:7], s[0:1], 0x38
	s_load_dword s34, s[0:1], 0x10
	s_load_dwordx4 s[16:19], s[0:1], 0x0
	s_load_dwordx8 s[8:15], s[0:1], 0x18
	s_load_dword s33, s[0:1], 0x48
	s_waitcnt lgkmcnt(0)
	s_mul_i32 s3, s5, s4
	s_mul_i32 s20, s3, s6
	s_cmp_ge_i32 s2, s20
	v_readfirstlane_b32 s3, v0
	s_cbranch_scc1 .LBB4_20
	s_ashr_i32 s21, s20, 31
	s_lshr_b32 s0, s21, 29
	v_lshrrev_b32_e32 v5, 5, v0
	s_add_i32 s0, s20, s0
	v_lshlrev_b32_e32 v3, 4, v0
	v_and_b32_e32 v5, 4, v5
	v_lshrrev_b32_e32 v6, 3, v0
	v_lshrrev_b32_e32 v7, 2, v0
	v_lshrrev_b32_e32 v18, 1, v0
	v_lshlrev_b32_e32 v9, 1, v0
	s_ashr_i32 s0, s0, 3
	v_and_b32_e32 v2, 16, v0
	v_and_b32_e32 v4, 0x70, v3
	v_and_b32_e32 v7, 64, v7
	v_and_or_b32 v5, v6, 3, v5
	v_and_b32_e32 v8, 48, v18
	v_and_b32_e32 v9, 64, v9
	s_ff1_i32_b32 s50, s0
	s_lshl_b32 s0, s6, 3
	v_or3_b32 v7, v8, v7, v5
	v_bitop3_b32 v2, v9, v4, v2 bitop3:0x36
	s_ff1_i32_b32 s51, s0
	s_waitcnt lgkmcnt(0)
	v_mad_u64_u32 v[146:147], s[0:1], s34, v6, v[2:3]
	v_mad_u64_u32 v[148:149], s[0:1], s34, v7, v[2:3]
	v_or_b32_e32 v3, 0x2000, v3
	v_lshrrev_b32_e32 v4, 7, v3
	v_lshrrev_b32_e32 v3, 6, v3
	v_and_b32_e32 v3, 0xc0, v3
	v_or3_b32 v3, v8, v3, v5
	s_lshr_b32 s28, s3, 6
	v_mad_u64_u32 v[150:151], s[0:1], s34, v4, v[2:3]
	v_mad_u64_u32 v[152:153], s[0:1], s34, v3, v[2:3]
	s_lshl_b32 s0, s28, 10
	s_add_i32 s54, s0, 0
	s_and_b32 s0, s2, 7
	s_lshl_b32 s0, s0, s50
	s_ashr_i32 s1, s2, 3
	s_add_i32 s0, s0, s1
	s_lshl_b32 s30, -1, s51
	s_ashr_i32 s1, s0, s51
	s_andn2_b32 s0, s0, s30
	s_lshl_b32 s1, s1, 3
	s_and_b32 s28, s0, 7
	s_ashr_i32 s35, s34, 31
	s_ff1_i32_b32 s52, s5
	s_or_b32 s77, s1, s28
	s_bfe_u32 s4, s3, 0x20006
	s_lshr_b32 s15, s3, 8
	s_lshl_b64 s[22:23], s[34:35], 7
	s_lshl_b64 s[24:25], s[34:35], 3
	s_lshl_b64 s[26:27], s[34:35], 8
	s_lshr_b32 s76, s0, 3
	s_ashr_i32 s0, s77, s52
	s_add_i32 s1, s5, -1
	s_cmp_lg_u32 s7, 0
	s_cselect_b32 s7, s1, -1
	s_and_b32 s5, s77, s7
	s_mul_i32 s0, s0, s6
	s_add_i32 s28, s0, s76
	s_ashr_i32 s0, s5, 31
	s_mul_i32 s0, s26, s0
	s_mul_hi_u32 s1, s26, s5
	s_add_i32 s29, s1, s0
	s_lshr_b64 s[0:1], s[34:35], 24
	s_mul_i32 s1, s0, s5
	s_add_i32 s31, s29, s1
	s_ashr_i32 s29, s28, 31
	s_mul_i32 s36, s26, s5
	s_mul_i32 s1, s26, s29
	s_mul_hi_u32 s5, s26, s28
	s_add_i32 s1, s5, s1
	s_mul_i32 s0, s0, s28
	s_add_i32 s1, s1, s0
	s_mul_i32 s0, s26, s28
	s_add_u32 s38, s18, s0
	v_bfe_u32 v1, v0, 4, 2
	s_addc_u32 s39, s19, s1
	s_lshl_b64 s[0:1], s[28:29], 10
	v_lshlrev_b32_e32 v2, 6, v1
	s_add_u32 s0, s10, s0
	v_lshl_or_b32 v147, s4, 8, v2
	s_addc_u32 s1, s11, s1
	global_load_dwordx4 v[14:17], v147, s[0:1]
	global_load_dwordx4 v[10:13], v147, s[0:1] offset:16
	global_load_dwordx4 v[6:9], v147, s[0:1] offset:32
	global_load_dwordx4 v[2:5], v147, s[0:1] offset:48
	s_add_i32 s55, s54, 0x10000
	s_mov_b32 m0, s55
	s_nop 0
	global_load_lds_dwordx4 v148, s[38:39]
	s_add_i32 s56, s54, 0x12000
	s_mov_b32 m0, s56
	s_nop 0
	global_load_lds_dwordx4 v152, s[38:39]
	s_add_u32 s40, s16, s36
	s_addc_u32 s41, s17, s31
	s_mov_b32 m0, s54
	s_nop 0
	global_load_lds_dwordx4 v146, s[40:41]
	s_add_i32 s57, s54, 0x2000
	s_add_i32 s58, s54, 0x14000
	s_mov_b32 m0, s57
	s_nop 0
	global_load_lds_dwordx4 v150, s[40:41]
	s_add_u32 s0, s38, s24
	s_addc_u32 s1, s39, s25
	s_mov_b32 m0, s58
	s_nop 0
	global_load_lds_dwordx4 v148, s[0:1]
	s_add_i32 s59, s54, 0x16000
	s_add_i32 s60, s54, 0x4000
	s_mov_b32 m0, s59
	s_nop 0
	global_load_lds_dwordx4 v152, s[0:1]
	s_add_u32 s36, s40, s22
	s_addc_u32 s37, s41, s23
	s_mov_b32 m0, s60
	s_nop 0
	global_load_lds_dwordx4 v146, s[36:37]
	s_add_i32 s61, s54, 0x6000
	s_mov_b32 m0, s61
	s_nop 0
	global_load_lds_dwordx4 v150, s[36:37]
	s_mov_b32 s53, 0
	s_mov_b32 s5, 0x10000
	s_cmp_lg_u32 s15, 1
	s_cbranch_scc1 .LBB4_3

_Z6k_gemmI4Epi8ILi1ELb1ELb1EEEv4GemmT_iiii:
	s_load_dwordx4 s[4:7], s[0:1], 0x38
	s_load_dword s34, s[0:1], 0x10
	s_load_dwordx4 s[16:19], s[0:1], 0x0
	s_load_dwordx8 s[8:15], s[0:1], 0x18
	s_load_dword s33, s[0:1], 0x48
	s_waitcnt lgkmcnt(0)
	s_mul_i32 s3, s5, s4
	s_mul_i32 s20, s3, s6
	s_cmp_ge_i32 s2, s20
	v_readfirstlane_b32 s3, v0
	s_cbranch_scc1 .LBB5_20
	s_ashr_i32 s21, s20, 31
	s_lshr_b32 s0, s21, 29
	v_lshrrev_b32_e32 v5, 5, v0
	s_add_i32 s0, s20, s0
	v_lshlrev_b32_e32 v3, 4, v0
	v_and_b32_e32 v5, 4, v5
	v_lshrrev_b32_e32 v6, 3, v0
	v_lshrrev_b32_e32 v7, 2, v0
	v_lshrrev_b32_e32 v18, 1, v0
	v_lshlrev_b32_e32 v9, 1, v0
	s_ashr_i32 s0, s0, 3
	v_and_b32_e32 v2, 16, v0
	v_and_b32_e32 v4, 0x70, v3
	v_and_b32_e32 v7, 64, v7
	v_and_or_b32 v5, v6, 3, v5
	v_and_b32_e32 v8, 48, v18
	v_and_b32_e32 v9, 64, v9
	s_ff1_i32_b32 s37, s0
	s_lshl_b32 s0, s6, 3
	v_or3_b32 v7, v8, v7, v5
	v_bitop3_b32 v2, v9, v4, v2 bitop3:0x36
	s_ff1_i32_b32 s52, s0
	s_waitcnt lgkmcnt(0)
	v_mad_u64_u32 v[146:147], s[0:1], s34, v6, v[2:3]
	v_mad_u64_u32 v[148:149], s[0:1], s34, v7, v[2:3]
	v_or_b32_e32 v3, 0x2000, v3
	v_lshrrev_b32_e32 v4, 7, v3
	v_lshrrev_b32_e32 v3, 6, v3
	v_and_b32_e32 v3, 0xc0, v3
	v_or3_b32 v3, v8, v3, v5
	s_lshr_b32 s28, s3, 6
	v_mad_u64_u32 v[150:151], s[0:1], s34, v4, v[2:3]
	v_mad_u64_u32 v[152:153], s[0:1], s34, v3, v[2:3]
	s_lshl_b32 s0, s28, 10
	s_add_i32 s55, s0, 0
	s_and_b32 s0, s2, 7
	s_lshl_b32 s0, s0, s37
	s_ashr_i32 s1, s2, 3
	s_add_i32 s0, s0, s1
	s_lshl_b32 s30, -1, s52
	s_ashr_i32 s1, s0, s52
	s_andn2_b32 s0, s0, s30
	s_lshl_b32 s1, s1, 3
	s_and_b32 s28, s0, 7
	s_ashr_i32 s35, s34, 31
	s_ff1_i32_b32 s53, s5
	s_or_b32 s78, s1, s28
	s_bfe_u32 s4, s3, 0x20006
	s_lshr_b32 s15, s3, 8
	s_lshl_b64 s[22:23], s[34:35], 7
	s_lshl_b64 s[24:25], s[34:35], 3
	s_lshl_b64 s[26:27], s[34:35], 8
	s_lshr_b32 s77, s0, 3
	s_ashr_i32 s0, s78, s53
	s_add_i32 s1, s5, -1
	s_cmp_lg_u32 s7, 0
	s_cselect_b32 s7, s1, -1
	s_and_b32 s5, s78, s7
	s_mul_i32 s0, s0, s6
	s_add_i32 s28, s0, s77
	s_ashr_i32 s0, s5, 31
	s_mul_i32 s0, s26, s0
	s_mul_hi_u32 s1, s26, s5
	s_add_i32 s29, s1, s0
	s_lshr_b64 s[0:1], s[34:35], 24
	s_mul_i32 s1, s0, s5
	s_add_i32 s31, s29, s1
	s_ashr_i32 s29, s28, 31
	s_mul_i32 s36, s26, s5
	s_mul_i32 s1, s26, s29
	s_mul_hi_u32 s5, s26, s28
	s_add_i32 s1, s5, s1
	s_mul_i32 s0, s0, s28
	s_add_i32 s1, s1, s0
	s_mul_i32 s0, s26, s28
	s_add_u32 s40, s18, s0
	v_bfe_u32 v1, v0, 4, 2
	s_addc_u32 s41, s19, s1
	s_lshl_b64 s[0:1], s[28:29], 10
	v_lshlrev_b32_e32 v2, 6, v1
	s_add_u32 s0, s10, s0
	v_lshl_or_b32 v147, s4, 8, v2
	s_addc_u32 s1, s11, s1
	global_load_dwordx4 v[14:17], v147, s[0:1]
	global_load_dwordx4 v[10:13], v147, s[0:1] offset:16
	global_load_dwordx4 v[6:9], v147, s[0:1] offset:32
	global_load_dwordx4 v[2:5], v147, s[0:1] offset:48
	s_add_i32 s56, s55, 0x10000
	s_mov_b32 m0, s56
	s_nop 0
	global_load_lds_dwordx4 v148, s[40:41]
	s_add_i32 s57, s55, 0x12000
	s_mov_b32 m0, s57
	s_nop 0
	global_load_lds_dwordx4 v152, s[40:41]
	s_add_u32 s42, s16, s36
	s_addc_u32 s43, s17, s31
	s_mov_b32 m0, s55
	s_nop 0
	global_load_lds_dwordx4 v146, s[42:43]
	s_add_i32 s58, s55, 0x2000
	s_add_i32 s59, s55, 0x14000
	s_mov_b32 m0, s58
	s_nop 0
	global_load_lds_dwordx4 v150, s[42:43]
	s_add_u32 s0, s40, s24
	s_addc_u32 s1, s41, s25
	s_mov_b32 m0, s59
	s_nop 0
	global_load_lds_dwordx4 v148, s[0:1]
	s_add_i32 s60, s55, 0x16000
	s_add_i32 s61, s55, 0x4000
	s_mov_b32 m0, s60
	s_nop 0
	global_load_lds_dwordx4 v152, s[0:1]
	s_add_u32 s38, s42, s22
	s_addc_u32 s39, s43, s23
	s_mov_b32 m0, s61
	s_nop 0
	global_load_lds_dwordx4 v146, s[38:39]
	s_add_i32 s62, s55, 0x6000
	s_mov_b32 m0, s62
	s_nop 0
	global_load_lds_dwordx4 v150, s[38:39]
	s_mov_b32 s54, 0
	s_mov_b32 s5, 0x10000
	s_cmp_lg_u32 s15, 1
	s_cbranch_scc1 .LBB5_3

amdhsa.kernels:
  - .agpr_count:     0
    .args:
      - .offset:         0
        .size:           80
        .value_kind:     by_value
    .group_segment_fixed_size: 8192
    .kernarg_segment_align: 8
    .kernarg_segment_size: 80
    .language:       OpenCL C
    .language_version:
      - 2
      - 0
    .max_flat_workgroup_size: 256
    .name:           _Z6k_prep8PrepArgs
    .private_segment_fixed_size: 0
    .sgpr_count:     35
    .sgpr_spill_count: 0
    .symbol:         _Z6k_prep8PrepArgs.kd
    .uniform_work_group_size: 1
    .uses_dynamic_stack: false
    .vgpr_count:     45
    .vgpr_spill_count: 0
    .wavefront_size: 64
  - .agpr_count:     4
    .args:
      - .actual_access:  read_only
        .address_space:  global
        .offset:         0
        .size:           8
        .value_kind:     global_buffer
      - .actual_access:  read_only
        .address_space:  global
        .offset:         8
        .size:           8
        .value_kind:     global_buffer
      - .actual_access:  read_only
        .address_space:  global
        .offset:         16
        .size:           8
        .value_kind:     global_buffer
      - .actual_access:  write_only
        .address_space:  global
        .offset:         24
        .size:           8
        .value_kind:     global_buffer
      - .actual_access:  write_only
        .address_space:  global
        .offset:         32
        .size:           8
        .value_kind:     global_buffer
    .group_segment_fixed_size: 36096
    .kernarg_segment_align: 8
    .kernarg_segment_size: 40
    .language:       OpenCL C
    .language_version:
      - 2
      - 0
    .max_flat_workgroup_size: 256
    .name:           _Z7k_gatesPKfPKtS0_PhPf
    .private_segment_fixed_size: 0
    .sgpr_count:     18
    .sgpr_spill_count: 0
    .symbol:         _Z7k_gatesPKfPKtS0_PhPf.kd
    .uniform_work_group_size: 1
    .uses_dynamic_stack: false
    .vgpr_count:     124
    .vgpr_spill_count: 0
    .wavefront_size: 64
  - .agpr_count:     0
    .args:
      - .actual_access:  read_only
        .address_space:  global
        .offset:         0
        .size:           8
        .value_kind:     global_buffer
      - .actual_access:  read_only
        .address_space:  global
        .offset:         8
        .size:           8
        .value_kind:     global_buffer
      - .actual_access:  write_only
        .address_space:  global
        .offset:         16
        .size:           8
        .value_kind:     global_buffer
      - .offset:         24
        .size:           4
        .value_kind:     by_value
    .group_segment_fixed_size: 0
    .kernarg_segment_align: 8
    .kernarg_segment_size: 28
    .language:       OpenCL C
    .language_version:
      - 2
      - 0
    .max_flat_workgroup_size: 256
    .name:           _Z5k_mixPKhPKfPhi
    .private_segment_fixed_size: 0
    .sgpr_count:     40
    .sgpr_spill_count: 0
    .symbol:         _Z5k_mixPKhPKfPhi.kd
    .uniform_work_group_size: 1
    .uses_dynamic_stack: false
    .vgpr_count:     124
    .vgpr_spill_count: 0
    .wavefront_size: 64
  - .agpr_count:     0
    .args:
      - .actual_access:  read_only
        .address_space:  global
        .offset:         0
        .size:           8
        .value_kind:     global_buffer
      - .actual_access:  read_only
        .address_space:  global
        .offset:         8
        .size:           8
        .value_kind:     global_buffer
      - .actual_access:  write_only
        .address_space:  global
        .offset:         16
        .size:           8
        .value_kind:     global_buffer
    .group_segment_fixed_size: 0
    .kernarg_segment_align: 8
    .kernarg_segment_size: 24
    .language:       OpenCL C
    .language_version:
      - 2
      - 0
    .max_flat_workgroup_size: 256
    .name:           _Z7k_finalPKfS0_Pf
    .private_segment_fixed_size: 0
    .sgpr_count:     16
    .sgpr_spill_count: 0
    .symbol:         _Z7k_finalPKfS0_Pf.kd
    .uniform_work_group_size: 1
    .uses_dynamic_stack: false
    .vgpr_count:     16
    .vgpr_spill_count: 0
    .wavefront_size: 64
  - .agpr_count:     0
    .args:
      - .offset:         0
        .size:           24
        .value_kind:     by_value
      - .offset:         24
        .size:           32
        .value_kind:     by_value
      - .offset:         56
        .size:           4
        .value_kind:     by_value
      - .offset:         60
        .size:           4
        .value_kind:     by_value
      - .offset:         64
        .size:           4
        .value_kind:     by_value
      - .offset:         68
        .size:           4
        .value_kind:     by_value
      - .offset:         72
        .size:           4
        .value_kind:     hidden_block_count_x
      - .offset:         76
        .size:           4
        .value_kind:     hidden_block_count_y
      - .offset:         80
        .size:           4
        .value_kind:     hidden_block_count_z
      - .offset:         84
        .size:           2
        .value_kind:     hidden_group_size_x
      - .offset:         86
        .size:           2
        .value_kind:     hidden_group_size_y
      - .offset:         88
        .size:           2
        .value_kind:     hidden_group_size_z
      - .offset:         90
        .size:           2
        .value_kind:     hidden_remainder_x
      - .offset:         92
        .size:           2
        .value_kind:     hidden_remainder_y
      - .offset:         94
        .size:           2
        .value_kind:     hidden_remainder_z
      - .offset:         112
        .size:           8
        .value_kind:     hidden_global_offset_x
      - .offset:         120
        .size:           8
        .value_kind:     hidden_global_offset_y
      - .offset:         128
        .size:           8
        .value_kind:     hidden_global_offset_z
      - .offset:         136
        .size:           2
        .value_kind:     hidden_grid_dims
      - .offset:         192
        .size:           4
        .value_kind:     hidden_dynamic_lds_size
    .group_segment_fixed_size: 0
    .kernarg_segment_align: 8
    .kernarg_segment_size: 328
    .language:       OpenCL C
    .language_version:
      - 2
      - 0
    .max_flat_workgroup_size: 512
    .name:           _Z6k_gemmI4Epi8ILi0ELb1ELb1EEEv4GemmT_iiii
    .private_segment_fixed_size: 0
    .sgpr_count:     92
    .sgpr_spill_count: 0
    .symbol:         _Z6k_gemmI4Epi8ILi0ELb1ELb1EEEv4GemmT_iiii.kd
    .uniform_work_group_size: 1
    .uses_dynamic_stack: false
    .vgpr_count:     248
    .vgpr_spill_count: 0
    .wavefront_size: 64
  - .agpr_count:     0
    .args:
      - .offset:         0
        .size:           24
        .value_kind:     by_value
      - .offset:         24
        .size:           32
        .value_kind:     by_value
      - .offset:         56
        .size:           4
        .value_kind:     by_value
      - .offset:         60
        .size:           4
        .value_kind:     by_value
      - .offset:         64
        .size:           4
        .value_kind:     by_value
      - .offset:         68
        .size:           4
        .value_kind:     by_value
      - .offset:         72
        .size:           4
        .value_kind:     hidden_block_count_x
      - .offset:         76
        .size:           4
        .value_kind:     hidden_block_count_y
      - .offset:         80
        .size:           4
        .value_kind:     hidden_block_count_z
      - .offset:         84
        .size:           2
        .value_kind:     hidden_group_size_x
      - .offset:         86
        .size:           2
        .value_kind:     hidden_group_size_y
      - .offset:         88
        .size:           2
        .value_kind:     hidden_group_size_z
      - .offset:         90
        .size:           2
        .value_kind:     hidden_remainder_x
      - .offset:         92
        .size:           2
        .value_kind:     hidden_remainder_y
      - .offset:         94
        .size:           2
        .value_kind:     hidden_remainder_z
      - .offset:         112
        .size:           8
        .value_kind:     hidden_global_offset_x
      - .offset:         120
        .size:           8
        .value_kind:     hidden_global_offset_y
      - .offset:         128
        .size:           8
        .value_kind:     hidden_global_offset_z
      - .offset:         136
        .size:           2
        .value_kind:     hidden_grid_dims
      - .offset:         192
        .size:           4
        .value_kind:     hidden_dynamic_lds_size
    .group_segment_fixed_size: 0
    .kernarg_segment_align: 8
    .kernarg_segment_size: 328
    .language:       OpenCL C
    .language_version:
      - 2
      - 0
    .max_flat_workgroup_size: 512
    .name:           _Z6k_gemmI4Epi8ILi1ELb1ELb1EEEv4GemmT_iiii
    .private_segment_fixed_size: 0
    .sgpr_count:     90
    .sgpr_spill_count: 0
    .symbol:         _Z6k_gemmI4Epi8ILi1ELb1ELb1EEEv4GemmT_iiii.kd
    .uniform_work_group_size: 1
    .uses_dynamic_stack: false
    .vgpr_count:     228
    .vgpr_spill_count: 0
    .wavefront_size: 64
  - .agpr_count:     0
    .args:
      - .offset:         0
        .size:           24
        .value_kind:     by_value
      - .offset:         24
        .size:           32
        .value_kind:     by_value
      - .offset:         56
        .size:           4
        .value_kind:     by_value
      - .offset:         60
        .size:           4
        .value_kind:     by_value
      - .offset:         64
        .size:           4
        .value_kind:     by_value
      - .offset:         68
        .size:           4
        .value_kind:     by_value
      - .offset:         72
        .size:           4
        .value_kind:     hidden_block_count_x
      - .offset:         76
        .size:           4
        .value_kind:     hidden_block_count_y
      - .offset:         80
        .size:           4
        .value_kind:     hidden_block_count_z
      - .offset:         84
        .size:           2
        .value_kind:     hidden_group_size_x
      - .offset:         86
        .size:           2
        .value_kind:     hidden_group_size_y
      - .offset:         88
        .size:           2
        .value_kind:     hidden_group_size_z
      - .offset:         90
        .size:           2
        .value_kind:     hidden_remainder_x
      - .offset:         92
        .size:           2
        .value_kind:     hidden_remainder_y
      - .offset:         94
        .size:           2
        .value_kind:     hidden_remainder_z
      - .offset:         112
        .size:           8
        .value_kind:     hidden_global_offset_x
      - .offset:         120
        .size:           8
        .value_kind:     hidden_global_offset_y
      - .offset:         128
        .size:           8
        .value_kind:     hidden_global_offset_z
      - .offset:         136
        .size:           2
        .value_kind:     hidden_grid_dims
      - .offset:         192
        .size:           4
        .value_kind:     hidden_dynamic_lds_size
    .group_segment_fixed_size: 0
    .kernarg_segment_align: 8
    .kernarg_segment_size: 328
    .language:       OpenCL C
    .language_version:
      - 2
      - 0
    .max_flat_workgroup_size: 512
    .name:           _Z6k_gemmI8EpiTowerEv4GemmT_iiii
    .private_segment_fixed_size: 0
    .sgpr_count:     92
    .sgpr_spill_count: 0
    .symbol:         _Z6k_gemmI8EpiTowerEv4GemmT_iiii.kd
    .uniform_work_group_size: 1
    .uses_dynamic_stack: false
    .vgpr_count:     230
    .vgpr_spill_count: 0
    .wavefront_size: 64
